# nt hint also on once-read streams: branch-gate bytes in the merge epilogue, final combine loads, layer-0 residual base loads, rmsnorm row loads
# baseline (speedup 1.0000x reference)
.LBB0_50:
	s_or_b64 exec, exec, s[2:3]
	v_readlane_b32 s6, v255, 36
	v_readlane_b32 s7, v255, 37
	s_mov_b64 s[2:3], -1
	s_and_b64 vcc, exec, s[6:7]
	v_ashrrev_i32_e32 v35, 31, v34
	s_cbranch_vccz .LBB0_57
	v_readlane_b32 s2, v254, 29
	s_cmpk_gt_i32 s46, 0x7fff
	s_mov_b32 s10, 0x1b400000
	v_mov_b32_e32 v0, s2
	v_readlane_b32 s2, v254, 30
	ds_read_b32 v0, v0
	s_mov_b32 s11, 0x23400000
	v_mov_b32_e32 v1, s2
	ds_read_b32 v1, v1
	s_waitcnt lgkmcnt(1)
	v_readfirstlane_b32 s2, v0
	s_waitcnt lgkmcnt(0)
	v_readfirstlane_b32 s3, v1
	s_cbranch_scc1 .LBB0_56
	s_ashr_i32 s47, s46, 31
	v_lshl_add_u64 v[0:1], v[34:35], 4, s[2:3]
	s_lshl_b64 s[2:3], s[46:47], 11
	s_add_u32 s6, s36, s2
	s_addc_u32 s7, s37, s3
	s_waitcnt vmcnt(1)
	v_lshlrev_b64 v[16:17], 3, v[34:35]
	v_lshl_add_u64 v[2:3], s[6:7], 0, v[16:17]
	s_mov_b64 s[6:7], 0x2400000
	v_add_co_u32_e32 v8, vcc, 0x1000, v0
	v_lshl_add_u64 v[4:5], v[2:3], 0, s[6:7]
	s_mov_b32 s6, 0x2400000
	s_mov_b64 s[34:35], vcc
	v_add_co_u32_e32 v2, vcc, s6, v2
	s_mov_b64 s[6:7], 0x1000
	s_nop 0
	v_addc_co_u32_e32 v3, vcc, 0, v3, vcc
	v_lshl_add_u64 v[12:13], v[0:1], 0, s[6:7]
	v_addc_co_u32_e64 v9, vcc, 0, v1, s[34:35]
	global_load_dwordx2 v[18:19], v[4:5], off offset:512 nt
	global_load_dwordx2 v[24:25], v[4:5], off offset:1024 nt
	global_load_dwordx2 v[28:29], v[2:3], off nt
	global_load_dwordx2 v[30:31], v[4:5], off offset:1536 nt
	s_nop 0
	global_load_dwordx4 v[0:3], v[12:13], off offset:1024
	global_load_dwordx4 v[4:7], v[12:13], off offset:2048
	s_nop 0
	global_load_dwordx4 v[8:11], v[8:9], off
	s_nop 0
	global_load_dwordx4 v[12:15], v[12:13], off offset:3072
	v_lshl_add_u64 v[36:37], s[2:3], 0, v[16:17]
	s_lshl_b64 s[2:3], s[46:47], 10
	s_mov_b32 s6, s46
	v_lshl_add_u64 v[38:39], v[34:35], 2, s[2:3]
	s_waitcnt vmcnt(7)
	v_lshlrev_b32_e32 v16, 16, v18
	v_and_b32_e32 v17, 0xffff0000, v18
	v_lshlrev_b32_e32 v20, 16, v19
	v_and_b32_e32 v19, 0xffff0000, v19
	s_waitcnt vmcnt(6)
	v_lshlrev_b32_e32 v22, 16, v24
	v_and_b32_e32 v23, 0xffff0000, v24
	v_lshlrev_b32_e32 v26, 16, v25
	v_and_b32_e32 v27, 0xffff0000, v25
	s_waitcnt vmcnt(5)
	v_lshlrev_b32_e32 v18, 16, v28
	v_and_b32_e32 v21, 0xffff0000, v28
	v_lshlrev_b32_e32 v24, 16, v29
	v_and_b32_e32 v25, 0xffff0000, v29
	s_waitcnt vmcnt(4)
	v_lshlrev_b32_e32 v28, 16, v30
	v_and_b32_e32 v29, 0xffff0000, v30
	v_lshlrev_b32_e32 v30, 16, v31
	v_and_b32_e32 v31, 0xffff0000, v31
	v_mov_b32_e32 v50, v16
	v_mov_b32_e32 v51, v17
	v_mov_b32_e32 v48, v20
	v_mov_b32_e32 v49, v19
	v_mov_b32_e32 v46, v22
	v_mov_b32_e32 v47, v23
	v_mov_b32_e32 v42, v26
	v_mov_b32_e32 v43, v27
	v_mov_b32_e32 v54, v18
	v_mov_b32_e32 v55, v21
	v_mov_b32_e32 v52, v24
	v_mov_b32_e32 v53, v25
	v_mov_b32_e32 v44, v28
	v_mov_b32_e32 v45, v29
	v_mov_b32_e32 v40, v30
	v_mov_b32_e32 v41, v31
	s_branch .LBB0_54

.LBB0_54:
	s_cmpk_gt_i32 s6, 0x77ff
	s_cselect_b64 s[2:3], -1, 0
	s_and_b64 vcc, exec, s[2:3]
	v_lshl_add_u64 v[56:57], s[36:37], 0, v[36:37]
	s_cbranch_vccnz .LBB0_53
	v_add_co_u32_e32 v16, vcc, 0x2800000, v56
	s_nop 1
	v_addc_co_u32_e32 v17, vcc, 0, v57, vcc
	global_load_dwordx2 v[22:23], v[16:17], off nt
	global_load_dwordx2 v[26:27], v[16:17], off offset:512 nt
	global_load_dwordx2 v[28:29], v[16:17], off offset:1024 nt
	global_load_dwordx2 v[30:31], v[16:17], off offset:1536 nt
	s_waitcnt vmcnt(3)
	v_lshlrev_b32_e32 v18, 16, v22
	v_and_b32_e32 v21, 0xffff0000, v22
	v_lshlrev_b32_e32 v24, 16, v23
	v_and_b32_e32 v25, 0xffff0000, v23
	s_waitcnt vmcnt(2)
	v_lshlrev_b32_e32 v16, 16, v26
	v_and_b32_e32 v17, 0xffff0000, v26
	v_lshlrev_b32_e32 v20, 16, v27
	v_and_b32_e32 v19, 0xffff0000, v27
	s_waitcnt vmcnt(1)
	v_lshlrev_b32_e32 v22, 16, v28
	v_and_b32_e32 v23, 0xffff0000, v28
	v_lshlrev_b32_e32 v26, 16, v29
	v_and_b32_e32 v27, 0xffff0000, v29
	s_waitcnt vmcnt(0)
	v_lshlrev_b32_e32 v28, 16, v30
	v_and_b32_e32 v29, 0xffff0000, v30
	v_lshlrev_b32_e32 v30, 16, v31
	v_and_b32_e32 v31, 0xffff0000, v31
	s_branch .LBB0_53

.LBB0_57:
	s_andn2_b64 vcc, exec, s[2:3]
	s_cbranch_vccnz .LBB0_63
	v_readlane_b32 s2, v254, 31
	v_readlane_b32 s6, v254, 30
	s_cmpk_gt_i32 s46, 0x7fff
	v_mov_b32_e32 v0, s2
	v_readlane_b32 s2, v254, 32
	ds_read_b32 v0, v0
	s_nop 0
	v_mov_b32_e32 v1, s2
	ds_read_b32 v1, v1
	v_readlane_b32 s2, v254, 29
	s_waitcnt lgkmcnt(0)
	v_readfirstlane_b32 s3, v1
	v_mov_b32_e32 v2, s2
	v_readfirstlane_b32 s2, v0
	v_mov_b32_e32 v1, s6
	ds_read_b32 v0, v2
	ds_read_b32 v1, v1
	s_waitcnt lgkmcnt(1)
	v_readfirstlane_b32 s18, v0
	s_waitcnt lgkmcnt(0)
	v_readfirstlane_b32 s19, v1
	s_cbranch_scc1 .LBB0_63
	s_ashr_i32 s47, s46, 31
	s_lshl_b64 s[6:7], s[46:47], 12
	s_add_u32 s2, s2, s6
	s_waitcnt vmcnt(3)
	v_lshlrev_b64 v[8:9], 4, v[34:35]
	s_addc_u32 s3, s3, s7
	v_lshl_add_u64 v[40:41], s[2:3], 0, v[8:9]
	global_load_dwordx4 v[0:3], v[40:41], off nt
	global_load_dwordx4 v[4:7], v[40:41], off offset:1024 nt
	global_load_dwordx4 v[12:15], v[40:41], off offset:2048 nt
	v_lshl_add_u64 v[24:25], s[18:19], 0, v[8:9]
	global_load_dwordx4 v[28:31], v[40:41], off offset:3072 nt
	global_load_dwordx4 v[8:11], v[24:25], off
	global_load_dwordx4 v[16:19], v[24:25], off offset:1024
	global_load_dwordx4 v[20:23], v[24:25], off offset:2048
	s_nop 0
	global_load_dwordx4 v[24:27], v[24:25], off offset:3072
	s_lshl_b64 s[2:3], s[46:47], 10
	s_lshl_b64 s[10:11], s[46:47], 11
	v_lshl_add_u64 v[36:37], v[34:35], 2, s[2:3]
	s_mov_b64 s[2:3], 0x800000
	s_mov_b32 s6, s46
	v_lshl_add_u64 v[38:39], v[34:35], 3, s[10:11]
	v_lshl_add_u64 v[40:41], v[40:41], 0, s[2:3]
	s_mov_b32 s7, 0x1b400000
	s_mov_b32 s10, 0x23400000
	s_waitcnt vmcnt(4)
	v_mov_b32_e32 v44, v28
	v_mov_b32_e32 v56, v0
	v_mov_b32_e32 v57, v1
	v_mov_b32_e32 v54, v2
	v_mov_b32_e32 v55, v3
	v_mov_b32_e32 v52, v4
	v_mov_b32_e32 v53, v5
	v_mov_b32_e32 v50, v6
	v_mov_b32_e32 v51, v7
	v_mov_b32_e32 v48, v12
	v_mov_b32_e32 v49, v13
	v_mov_b32_e32 v46, v14
	v_mov_b32_e32 v47, v15
	v_mov_b32_e32 v45, v29
	v_mov_b32_e32 v42, v30
	v_mov_b32_e32 v43, v31
	s_branch .LBB0_61

.LBB0_61:
	s_cmpk_gt_i32 s6, 0x77ff
	s_cselect_b64 s[2:3], -1, 0
	s_and_b64 vcc, exec, s[2:3]
	s_cbranch_vccnz .LBB0_60
	global_load_dwordx4 v[0:3], v[40:41], off nt
	global_load_dwordx4 v[4:7], v[40:41], off offset:1024 nt
	global_load_dwordx4 v[12:15], v[40:41], off offset:2048 nt
	global_load_dwordx4 v[28:31], v[40:41], off offset:3072 nt
	s_branch .LBB0_60

.LBB0_400:
	v_readlane_b32 s2, v252, 1
	v_readlane_b32 s3, v252, 2
	s_waitcnt lgkmcnt(0)
	s_barrier
	v_mbcnt_lo_u32_b32 v0, -1, 0
	v_mbcnt_hi_u32_b32 v0, -1, v0
	v_readlane_b32 s6, v252, 6
	v_readlane_b32 s7, v252, 7
	s_add_i32 s6, s6, s7
	v_readlane_b32 s7, v254, 49
	s_mul_i32 s18, s72, 0x60
	s_mov_b32 s19, s97
	v_mov_b32_e32 v1, s7
	ds_read_b32 v1, v1
	v_readlane_b32 s7, v254, 50
	s_cmpk_gt_i32 s6, 0x7fff
	s_waitcnt lgkmcnt(0)
	v_readfirstlane_b32 s22, v1
	v_mov_b32_e32 v1, s7
	ds_read_b32 v1, v1
	s_waitcnt lgkmcnt(0)
	v_readfirstlane_b32 s23, v1
	s_cbranch_scc1 .LBB0_405
	s_add_u32 s10, s2, 0x180000
	s_addc_u32 s11, s3, 0
	s_add_u32 s34, s2, 0x1a0000
	s_addc_u32 s35, s3, 0
	s_lshl_b64 s[36:37], s[18:19], 2
	s_add_u32 s22, s22, s36
	v_ashrrev_i32_e32 v24, 3, v0
	v_and_b32_e32 v16, 7, v0
	v_lshlrev_b32_e32 v0, 4, v0
	s_addc_u32 s23, s23, s37
	s_lshl_b32 s31, s6, 6
	v_and_b32_e32 v8, 48, v0
	v_mov_b32_e32 v9, v161
	s_lshl_b32 s7, s6, 4
	s_and_b32 s31, s31, 0x1ffc0
	v_lshl_add_u64 v[38:39], s[34:35], 0, v[8:9]
	s_add_u32 s34, s34, s31
	s_addc_u32 s35, s35, 0
	v_lshl_add_u64 v[36:37], s[10:11], 0, v[8:9]
	s_add_u32 s10, s10, s31
	s_addc_u32 s11, s11, 0
	s_mul_i32 s33, s6, 0x1a00
	global_load_dwordx4 v[4:7], v8, s[34:35]
	s_mul_hi_i32 s31, s6, 0x1a00
	global_load_dwordx4 v[8:11], v8, s[10:11]
	s_add_u32 s10, s2, s33
	v_lshlrev_b32_e32 v160, 3, v16
	s_addc_u32 s11, s3, s31
	v_lshlrev_b32_e32 v12, 7, v24
	v_lshl_add_u64 v[14:15], s[10:11], 0, v[160:161]
	s_mov_b32 s10, 0x6400000
	s_mul_i32 s35, s6, 0xe00
	v_ashrrev_i32_e32 v13, 31, v12
	v_add_co_u32_e32 v14, vcc, s10, v14
	s_mul_hi_i32 s34, s6, 0xe00
	s_add_u32 s10, s2, s35
	s_addc_u32 s11, s3, s34
	v_lshlrev_b64 v[22:23], 1, v[12:13]
	v_lshlrev_b32_e32 v20, 4, v16
	v_lshl_add_u64 v[12:13], s[10:11], 0, v[22:23]
	v_mov_b32_e32 v21, v161
	v_addc_co_u32_e32 v15, vcc, 0, v15, vcc
	v_lshl_add_u64 v[12:13], v[12:13], 0, v[20:21]
	s_mov_b32 s10, 0x13400000
	v_add_co_u32_e32 v12, vcc, s10, v12
	global_load_dwordx2 v[50:51], v[14:15], off offset:3840 nt
	s_nop 0
	v_addc_co_u32_e32 v13, vcc, 0, v13, vcc
	global_load_dwordx4 v[32:35], v[12:13], off offset:1536 nt
	v_cmp_gt_u32_e64 s[40:41], 4, v16
	v_lshlrev_b32_e32 v16, 5, v16
	global_load_dwordx4 v[0:3], v20, s[22:23] offset:256
	global_load_dwordx4 v[12:15], v16, s[22:23]
	s_nop 0
	global_load_dwordx4 v[16:19], v16, s[22:23] offset:16
	s_movk_i32 s10, 0x60
	s_mul_i32 s11, s6, 0x600
	v_mul_lo_u32 v24, v24, s10
	s_mul_hi_i32 s10, s6, 0x600
	s_add_u32 s22, s11, 0x1a400080
	s_addc_u32 s23, s10, 0
	v_ashrrev_i32_e32 v25, 31, v24
	s_add_u32 s11, s11, 0x1a400000
	v_or_b32_e32 v26, s22, v160
	v_mov_b32_e32 v27, s23
	v_lshlrev_b64 v[24:25], 1, v[24:25]
	s_addc_u32 s10, s10, 0
	v_lshl_add_u64 v[40:41], v[26:27], 0, v[24:25]
	v_mov_b32_e32 v27, s10
	s_add_u32 s10, s33, 0x7100f00
	v_or_b32_e32 v26, s11, v20
	s_addc_u32 s11, s31, 0
	v_or_b32_e32 v44, s10, v160
	s_add_u32 s10, s35, 0x13b00600
	v_mov_b32_e32 v45, s11
	s_addc_u32 s11, s34, 0
	v_or_b32_e32 v20, s10, v20
	v_mov_b32_e32 v21, s11
	v_lshl_add_u64 v[42:43], v[26:27], 0, v[24:25]
	v_lshl_add_u64 v[46:47], v[20:21], 0, v[22:23]
	s_waitcnt vmcnt(6)
	v_mov_b64_e32 v[26:27], v[6:7]
	v_mov_b64_e32 v[24:25], v[4:5]
	s_waitcnt vmcnt(5)
	v_mov_b64_e32 v[30:31], v[10:11]
	v_mov_b64_e32 v[28:29], v[8:9]
	s_waitcnt vmcnt(4)
	v_mov_b64_e32 v[48:49], v[50:51]
	s_waitcnt vmcnt(3)
	v_mov_b64_e32 v[20:21], v[32:33]
	v_mov_b64_e32 v[22:23], v[34:35]
	s_branch .LBB0_403

.LBB0_403:
	s_cmpk_gt_i32 s6, 0x77ff
	s_cselect_b64 s[22:23], -1, 0
	s_and_b64 vcc, exec, s[22:23]
	s_cbranch_vccnz .LBB0_402
	s_and_b32 s10, s7, 0x7ff0
	v_lshl_add_u64 v[20:21], s[2:3], 0, v[46:47]
	v_lshl_add_u64 v[24:25], s[2:3], 0, v[44:45]
	s_lshl_b32 s96, s10, 2
	global_load_dwordx4 v[20:23], v[20:21], off nt
	s_nop 0
	global_load_dwordx2 v[48:49], v[24:25], off nt
	v_lshl_add_u64 v[24:25], v[36:37], 0, s[96:97]
	v_lshl_add_u64 v[26:27], v[38:39], 0, s[96:97]
	global_load_dwordx4 v[28:31], v[24:25], off
	s_nop 0
	global_load_dwordx4 v[24:27], v[26:27], off
	s_branch .LBB0_402

.LBB0_868:
	s_lshl_b32 s2, s38, 2
	s_ashr_i32 s3, s2, 31
	s_lshl_b64 s[92:93], s[2:3], 16
	s_cmp_lt_i32 s38, 3
	s_cselect_b64 s[22:23], -1, 0
	s_cmp_gt_i32 s38, 2
	s_cselect_b64 s[2:3], -1, 0
	s_add_u32 s90, s92, 0x40000
	s_addc_u32 s91, s93, 0
	s_lshl_b32 s39, s95, 4
	s_add_i32 s42, s39, s87
	s_ashr_i32 s43, s42, 31
	s_lshl_b64 s[42:43], s[42:43], 16
	v_lshl_add_u64 v[148:149], v[132:133], 0, s[42:43]
	v_mov_b64_e32 v[138:139], v[148:149]
	s_and_b64 vcc, exec, s[2:3]
	v_lshl_add_u64 v[136:137], v[138:139], 0, s[92:93]
	global_load_dwordx2 v[156:157], v[136:137], off nt
	v_lshl_add_u64 v[140:141], v[138:139], 0, s[90:91]
	s_cbranch_vccnz .LBB0_870
	global_load_dwordx2 v[146:147], v[140:141], off nt
.LBB0_870:
	global_load_dwordx2 v[154:155], v[136:137], off offset:512 nt
	v_cndmask_b32_e64 v138, 0, 1, s[22:23]
	v_cmp_ne_u32_e64 s[46:47], 1, v138
	s_andn2_b64 vcc, exec, s[22:23]
	s_cbranch_vccnz .LBB0_902
	global_load_dwordx2 v[144:145], v[140:141], off offset:512 nt
	global_load_dwordx2 v[152:153], v[136:137], off offset:1024 nt
	s_and_b64 vcc, exec, s[46:47]
	s_cbranch_vccz .LBB0_903
.LBB0_872:
	global_load_dwordx2 v[150:151], v[136:137], off offset:1536 nt
	s_and_b64 vcc, exec, s[46:47]
	s_cbranch_vccnz .LBB0_874
.LBB0_873:
	global_load_dwordx2 v[136:137], v[140:141], off offset:1536 nt

.LBB0_898:
	v_mov_b64_e32 v[152:153], v[148:149]
	s_and_b64 vcc, exec, s[46:47]
	v_lshl_add_u64 v[150:151], v[152:153], 0, s[92:93]
	global_load_dwordx2 v[158:159], v[150:151], off offset:2048 nt
	v_lshl_add_u64 v[156:157], v[152:153], 0, s[90:91]
	s_cbranch_vccnz .LBB0_904
	global_load_dwordx2 v[146:147], v[156:157], off offset:2048 nt
	global_load_dwordx2 v[154:155], v[150:151], off offset:2560 nt
	s_and_b64 vcc, exec, s[46:47]
	s_cbranch_vccz .LBB0_905
.LBB0_900:
	global_load_dwordx2 v[152:153], v[150:151], off offset:3072 nt
	s_and_b64 vcc, exec, s[46:47]
	s_cbranch_vccnz .LBB0_906
.LBB0_901:
	global_load_dwordx2 v[138:139], v[156:157], off offset:3072 nt
	s_nop 0
	global_load_dwordx2 v[150:151], v[150:151], off offset:3584 nt
	s_and_b64 vcc, exec, s[46:47]
	s_cbranch_vccz .LBB0_907
	s_branch .LBB0_908
.LBB0_902:
	global_load_dwordx2 v[152:153], v[136:137], off offset:1024 nt
	s_and_b64 vcc, exec, s[46:47]
	s_cbranch_vccnz .LBB0_872
.LBB0_903:
	global_load_dwordx2 v[138:139], v[140:141], off offset:1024 nt
	global_load_dwordx2 v[150:151], v[136:137], off offset:1536 nt
	s_and_b64 vcc, exec, s[46:47]
	s_cbranch_vccz .LBB0_873
	s_branch .LBB0_874
.LBB0_904:
	global_load_dwordx2 v[154:155], v[150:151], off offset:2560 nt
	s_and_b64 vcc, exec, s[46:47]
	s_cbranch_vccnz .LBB0_900
.LBB0_905:
	global_load_dwordx2 v[144:145], v[156:157], off offset:2560 nt
	global_load_dwordx2 v[152:153], v[150:151], off offset:3072 nt
	s_and_b64 vcc, exec, s[46:47]
	s_cbranch_vccz .LBB0_901
.LBB0_906:
	global_load_dwordx2 v[150:151], v[150:151], off offset:3584 nt
	s_and_b64 vcc, exec, s[46:47]
	s_cbranch_vccnz .LBB0_908
.LBB0_907:
	global_load_dwordx2 v[136:137], v[156:157], off offset:3584 nt

.LBB0_932:
	v_mov_b64_e32 v[150:151], v[148:149]
	s_mov_b64 s[2:3], 0x1000
	s_and_b64 vcc, exec, s[46:47]
	v_lshl_add_u64 v[152:153], v[150:151], 0, s[2:3]
	v_lshl_add_u64 v[154:155], v[152:153], 0, s[92:93]
	global_load_dwordx2 v[158:159], v[154:155], off nt
	s_cbranch_vccnz .LBB0_934
	v_lshl_add_u64 v[146:147], v[152:153], 0, s[90:91]
	global_load_dwordx2 v[146:147], v[146:147], off nt
.LBB0_934:
	s_mov_b64 s[2:3], 0x1200
	v_lshl_add_u64 v[152:153], v[150:151], 0, s[2:3]
	v_lshl_add_u64 v[154:155], v[152:153], 0, s[92:93]
	global_load_dwordx2 v[154:155], v[154:155], off nt
	s_and_b64 vcc, exec, s[46:47]
	s_cbranch_vccnz .LBB0_936
	v_lshl_add_u64 v[144:145], v[152:153], 0, s[90:91]
	global_load_dwordx2 v[144:145], v[144:145], off nt
.LBB0_936:
	s_mov_b64 s[2:3], 0x1400
	v_lshl_add_u64 v[156:157], v[150:151], 0, s[2:3]
	v_lshl_add_u64 v[152:153], v[156:157], 0, s[92:93]
	global_load_dwordx2 v[152:153], v[152:153], off nt
	s_and_b64 vcc, exec, s[46:47]
	s_cbranch_vccnz .LBB0_938
	v_lshl_add_u64 v[138:139], v[156:157], 0, s[90:91]
	global_load_dwordx2 v[138:139], v[138:139], off nt
.LBB0_938:
	s_mov_b64 s[2:3], 0x1600
	v_lshl_add_u64 v[156:157], v[150:151], 0, s[2:3]
	v_lshl_add_u64 v[150:151], v[156:157], 0, s[92:93]
	global_load_dwordx2 v[150:151], v[150:151], off nt
	s_and_b64 vcc, exec, s[46:47]
	s_cbranch_vccnz .LBB0_940
	v_lshl_add_u64 v[136:137], v[156:157], 0, s[90:91]
	global_load_dwordx2 v[136:137], v[136:137], off nt

.LBB0_964:
	s_mov_b64 s[2:3], 0x1800
	s_and_b64 vcc, exec, s[46:47]
	v_lshl_add_u64 v[150:151], v[148:149], 0, s[2:3]
	v_lshl_add_u64 v[152:153], v[150:151], 0, s[92:93]
	global_load_dwordx2 v[156:157], v[152:153], off nt
	s_cbranch_vccnz .LBB0_966
	v_lshl_add_u64 v[146:147], v[150:151], 0, s[90:91]
	global_load_dwordx2 v[146:147], v[146:147], off nt
.LBB0_966:
	s_mov_b64 s[2:3], 0x1a00
	v_lshl_add_u64 v[150:151], v[148:149], 0, s[2:3]
	v_lshl_add_u64 v[152:153], v[150:151], 0, s[92:93]
	global_load_dwordx2 v[152:153], v[152:153], off nt
	s_and_b64 vcc, exec, s[46:47]
	s_cbranch_vccnz .LBB0_968
	v_lshl_add_u64 v[144:145], v[150:151], 0, s[90:91]
	global_load_dwordx2 v[144:145], v[144:145], off nt
.LBB0_968:
	s_mov_b64 s[2:3], 0x1c00
	v_lshl_add_u64 v[154:155], v[148:149], 0, s[2:3]
	v_lshl_add_u64 v[150:151], v[154:155], 0, s[92:93]
	global_load_dwordx2 v[150:151], v[150:151], off nt
	s_and_b64 vcc, exec, s[46:47]
	s_cbranch_vccnz .LBB0_970
	v_lshl_add_u64 v[138:139], v[154:155], 0, s[90:91]
	global_load_dwordx2 v[138:139], v[138:139], off nt
.LBB0_970:
	s_mov_b64 s[2:3], 0x1e00
	v_lshl_add_u64 v[154:155], v[148:149], 0, s[2:3]
	v_lshl_add_u64 v[148:149], v[154:155], 0, s[92:93]
	global_load_dwordx2 v[148:149], v[148:149], off nt
	s_and_b64 vcc, exec, s[46:47]
	s_cbranch_vccnz .LBB0_972
	v_lshl_add_u64 v[136:137], v[154:155], 0, s[90:91]
	global_load_dwordx2 v[136:137], v[136:137], off nt

.LBB0_1097:
	v_lshl_add_u32 v132, s83, 8, v134
	v_lshl_or_b32 v158, s81, 8, v136
	v_ashrrev_i32_e32 v159, 31, v158
	v_ashrrev_i32_e32 v133, 31, v132
	v_lshl_add_u64 v[130:131], v[158:159], 2, s[18:19]
	v_lshlrev_b64 v[138:139], 12, v[132:133]
	v_or_b32_e32 v174, 16, v132
	v_lshl_add_u64 v[150:151], v[130:131], 0, v[138:139]
	v_ashrrev_i32_e32 v175, 31, v174
	global_load_dwordx4 v[138:141], v[150:151], off nt
	global_load_dwordx4 v[142:145], v[150:151], off offset:64 nt
	global_load_dwordx4 v[146:149], v[150:151], off offset:512 nt
	s_nop 0
	global_load_dwordx4 v[150:153], v[150:151], off offset:576 nt
	v_lshlrev_b64 v[154:155], 12, v[174:175]
	v_lshl_add_u64 v[170:171], v[130:131], 0, v[154:155]
	global_load_dwordx4 v[154:157], v[170:171], off nt
	global_load_dwordx4 v[162:165], v[170:171], off offset:64 nt
	global_load_dwordx4 v[166:169], v[170:171], off offset:512 nt
	s_nop 0
	global_load_dwordx4 v[170:173], v[170:171], off offset:576 nt
	s_mov_b64 s[2:3], -1
	s_andn2_b64 vcc, exec, s[40:41]
	s_waitcnt vmcnt(0)
	v_pk_add_f32 v[124:125], v[124:125], v[138:139]
	v_pk_add_f32 v[126:127], v[126:127], v[140:141]
	v_cvt_pk_bf16_f32 v138, v124, v125
	v_lshlrev_b64 v[124:125], 11, v[132:133]
	v_cvt_pk_bf16_f32 v139, v126, v127
	v_lshl_add_u64 v[126:127], s[34:35], 0, v[124:125]
	v_lshlrev_b64 v[124:125], 1, v[158:159]
	v_pk_add_f32 v[122:123], v[122:123], v[144:145]
	v_pk_add_f32 v[120:121], v[120:121], v[142:143]
	v_pk_add_f32 v[118:119], v[118:119], v[148:149]
	v_pk_add_f32 v[116:117], v[116:117], v[146:147]
	v_pk_add_f32 v[114:115], v[114:115], v[152:153]
	v_pk_add_f32 v[112:113], v[112:113], v[150:151]
	v_pk_add_f32 v[110:111], v[110:111], v[156:157]
	v_pk_add_f32 v[108:109], v[108:109], v[154:155]
	v_lshl_add_u64 v[126:127], v[126:127], 0, v[124:125]
	v_cvt_pk_bf16_f32 v120, v120, v121
	v_cvt_pk_bf16_f32 v121, v122, v123
	v_cvt_pk_bf16_f32 v116, v116, v117
	v_cvt_pk_bf16_f32 v117, v118, v119
	v_cvt_pk_bf16_f32 v112, v112, v113
	v_cvt_pk_bf16_f32 v113, v114, v115
	v_cvt_pk_bf16_f32 v108, v108, v109
	v_cvt_pk_bf16_f32 v109, v110, v111
	v_lshlrev_b64 v[110:111], 11, v[174:175]
	global_store_dwordx2 v[126:127], v[138:139], off nt
	global_store_dwordx2 v[126:127], v[120:121], off offset:32 nt
	global_store_dwordx2 v[126:127], v[116:117], off offset:256 nt
	global_store_dwordx2 v[126:127], v[112:113], off offset:288 nt
	v_lshl_add_u64 v[110:111], s[34:35], 0, v[110:111]
	v_pk_add_f32 v[106:107], v[106:107], v[164:165]
	v_pk_add_f32 v[104:105], v[104:105], v[162:163]
	v_pk_add_f32 v[102:103], v[102:103], v[168:169]
	v_pk_add_f32 v[100:101], v[100:101], v[166:167]
	v_pk_add_f32 v[98:99], v[98:99], v[172:173]
	v_pk_add_f32 v[96:97], v[96:97], v[170:171]
	v_or_b32_e32 v126, 32, v132
	v_or_b32_e32 v142, 48, v132
	v_lshl_add_u64 v[110:111], v[110:111], 0, v[124:125]
	v_cvt_pk_bf16_f32 v104, v104, v105
	v_cvt_pk_bf16_f32 v105, v106, v107
	v_cvt_pk_bf16_f32 v100, v100, v101
	v_cvt_pk_bf16_f32 v101, v102, v103
	v_cvt_pk_bf16_f32 v96, v96, v97
	v_cvt_pk_bf16_f32 v97, v98, v99
	v_ashrrev_i32_e32 v127, 31, v126
	v_ashrrev_i32_e32 v143, 31, v142
	global_store_dwordx2 v[110:111], v[108:109], off nt
	global_store_dwordx2 v[110:111], v[104:105], off offset:32 nt
	global_store_dwordx2 v[110:111], v[100:101], off offset:256 nt
	global_store_dwordx2 v[110:111], v[96:97], off offset:288 nt
	v_lshlrev_b64 v[96:97], 12, v[126:127]
	v_lshlrev_b64 v[112:113], 12, v[142:143]
	v_lshl_add_u64 v[108:109], v[130:131], 0, v[96:97]
	v_lshl_add_u64 v[138:139], v[130:131], 0, v[112:113]
	global_load_dwordx4 v[96:99], v[108:109], off nt
	global_load_dwordx4 v[100:103], v[108:109], off offset:64 nt
	global_load_dwordx4 v[104:107], v[108:109], off offset:512 nt
	s_nop 0
	global_load_dwordx4 v[108:111], v[108:109], off offset:576 nt
	s_nop 0
	global_load_dwordx4 v[112:115], v[138:139], off nt
	global_load_dwordx4 v[116:119], v[138:139], off offset:64 nt
	global_load_dwordx4 v[120:123], v[138:139], off offset:512 nt
	s_nop 0
	global_load_dwordx4 v[138:141], v[138:139], off offset:576 nt
	s_waitcnt vmcnt(0)
	v_pk_add_f32 v[94:95], v[94:95], v[98:99]
	v_pk_add_f32 v[92:93], v[92:93], v[96:97]
	v_pk_add_f32 v[78:79], v[78:79], v[114:115]
	v_pk_add_f32 v[76:77], v[76:77], v[112:113]
	v_cvt_pk_bf16_f32 v92, v92, v93
	v_cvt_pk_bf16_f32 v93, v94, v95
	v_lshlrev_b64 v[94:95], 11, v[126:127]
	v_cvt_pk_bf16_f32 v76, v76, v77
	v_cvt_pk_bf16_f32 v77, v78, v79
	v_lshlrev_b64 v[78:79], 11, v[142:143]
	v_lshl_add_u64 v[94:95], s[34:35], 0, v[94:95]
	v_pk_add_f32 v[90:91], v[90:91], v[102:103]
	v_pk_add_f32 v[88:89], v[88:89], v[100:101]
	v_pk_add_f32 v[86:87], v[86:87], v[106:107]
	v_pk_add_f32 v[84:85], v[84:85], v[104:105]
	v_pk_add_f32 v[82:83], v[82:83], v[110:111]
	v_pk_add_f32 v[80:81], v[80:81], v[108:109]
	v_lshl_add_u64 v[78:79], s[34:35], 0, v[78:79]
	v_pk_add_f32 v[74:75], v[74:75], v[118:119]
	v_pk_add_f32 v[72:73], v[72:73], v[116:117]
	v_pk_add_f32 v[70:71], v[70:71], v[122:123]
	v_pk_add_f32 v[68:69], v[68:69], v[120:121]
	v_pk_add_f32 v[66:67], v[66:67], v[140:141]
	v_pk_add_f32 v[64:65], v[64:65], v[138:139]
	v_add_u32_e32 v96, 0x80, v132
	v_add_u32_e32 v98, 0x90, v132
	v_lshl_add_u64 v[94:95], v[94:95], 0, v[124:125]
	v_cvt_pk_bf16_f32 v88, v88, v89
	v_cvt_pk_bf16_f32 v89, v90, v91
	v_cvt_pk_bf16_f32 v84, v84, v85
	v_cvt_pk_bf16_f32 v85, v86, v87
	v_cvt_pk_bf16_f32 v80, v80, v81
	v_cvt_pk_bf16_f32 v81, v82, v83
	v_lshl_add_u64 v[78:79], v[78:79], 0, v[124:125]
	v_cvt_pk_bf16_f32 v72, v72, v73
	v_cvt_pk_bf16_f32 v73, v74, v75
	v_cvt_pk_bf16_f32 v68, v68, v69
	v_cvt_pk_bf16_f32 v69, v70, v71
	v_cvt_pk_bf16_f32 v64, v64, v65
	v_cvt_pk_bf16_f32 v65, v66, v67
	v_ashrrev_i32_e32 v97, 31, v96
	v_ashrrev_i32_e32 v99, 31, v98
	global_store_dwordx2 v[94:95], v[92:93], off nt
	global_store_dwordx2 v[94:95], v[88:89], off offset:32 nt
	global_store_dwordx2 v[94:95], v[84:85], off offset:256 nt
	global_store_dwordx2 v[94:95], v[80:81], off offset:288 nt
	global_store_dwordx2 v[78:79], v[76:77], off nt
	global_store_dwordx2 v[78:79], v[72:73], off offset:32 nt
	global_store_dwordx2 v[78:79], v[68:69], off offset:256 nt
	global_store_dwordx2 v[78:79], v[64:65], off offset:288 nt
	v_lshlrev_b64 v[64:65], 12, v[96:97]
	v_lshlrev_b64 v[80:81], 12, v[98:99]
	v_lshl_add_u64 v[76:77], v[130:131], 0, v[64:65]
	v_lshl_add_u64 v[92:93], v[130:131], 0, v[80:81]
	global_load_dwordx4 v[64:67], v[76:77], off nt
	global_load_dwordx4 v[68:71], v[76:77], off offset:64 nt
	global_load_dwordx4 v[72:75], v[76:77], off offset:512 nt
	s_nop 0
	global_load_dwordx4 v[76:79], v[76:77], off offset:576 nt
	s_nop 0
	global_load_dwordx4 v[80:83], v[92:93], off nt
	global_load_dwordx4 v[84:87], v[92:93], off offset:64 nt
	global_load_dwordx4 v[88:91], v[92:93], off offset:512 nt
	s_nop 0
	global_load_dwordx4 v[92:95], v[92:93], off offset:576 nt
	s_waitcnt vmcnt(0)
	v_pk_add_f32 v[62:63], v[62:63], v[66:67]
	v_pk_add_f32 v[46:47], v[46:47], v[82:83]
	v_pk_add_f32 v[44:45], v[44:45], v[80:81]
	v_pk_add_f32 v[60:61], v[60:61], v[64:65]
	v_cvt_pk_bf16_f32 v44, v44, v45
	v_cvt_pk_bf16_f32 v45, v46, v47
	v_lshlrev_b64 v[46:47], 11, v[98:99]
	v_lshl_add_u64 v[46:47], s[34:35], 0, v[46:47]
	v_pk_add_f32 v[42:43], v[42:43], v[86:87]
	v_pk_add_f32 v[40:41], v[40:41], v[84:85]
	v_cvt_pk_bf16_f32 v60, v60, v61
	v_cvt_pk_bf16_f32 v61, v62, v63
	v_lshlrev_b64 v[62:63], 11, v[96:97]
	v_lshl_add_u64 v[46:47], v[46:47], 0, v[124:125]
	v_cvt_pk_bf16_f32 v40, v40, v41
	v_cvt_pk_bf16_f32 v41, v42, v43
	v_lshl_add_u64 v[62:63], s[34:35], 0, v[62:63]
	v_pk_add_f32 v[58:59], v[58:59], v[70:71]
	v_pk_add_f32 v[56:57], v[56:57], v[68:69]
	v_pk_add_f32 v[54:55], v[54:55], v[74:75]
	v_pk_add_f32 v[52:53], v[52:53], v[72:73]
	v_pk_add_f32 v[50:51], v[50:51], v[78:79]
	v_pk_add_f32 v[48:49], v[48:49], v[76:77]
	global_store_dwordx2 v[46:47], v[40:41], off offset:32 nt
	v_pk_add_f32 v[38:39], v[38:39], v[90:91]
	v_pk_add_f32 v[36:37], v[36:37], v[88:89]
	v_pk_add_f32 v[34:35], v[34:35], v[94:95]
	v_pk_add_f32 v[32:33], v[32:33], v[92:93]
	v_add_u32_e32 v40, 0xa0, v132
	v_lshl_add_u64 v[62:63], v[62:63], 0, v[124:125]
	v_cvt_pk_bf16_f32 v56, v56, v57
	v_cvt_pk_bf16_f32 v57, v58, v59
	v_cvt_pk_bf16_f32 v52, v52, v53
	v_cvt_pk_bf16_f32 v53, v54, v55
	v_cvt_pk_bf16_f32 v48, v48, v49
	v_cvt_pk_bf16_f32 v49, v50, v51
	v_cvt_pk_bf16_f32 v36, v36, v37
	v_cvt_pk_bf16_f32 v37, v38, v39
	v_cvt_pk_bf16_f32 v32, v32, v33
	v_cvt_pk_bf16_f32 v33, v34, v35
	v_ashrrev_i32_e32 v41, 31, v40
	global_store_dwordx2 v[62:63], v[60:61], off nt
	global_store_dwordx2 v[62:63], v[56:57], off offset:32 nt
	global_store_dwordx2 v[62:63], v[52:53], off offset:256 nt
	global_store_dwordx2 v[62:63], v[48:49], off offset:288 nt
	global_store_dwordx2 v[46:47], v[44:45], off nt
	global_store_dwordx2 v[46:47], v[36:37], off offset:256 nt
	global_store_dwordx2 v[46:47], v[32:33], off offset:288 nt
	v_lshlrev_b64 v[32:33], 12, v[40:41]
	v_add_u32_e32 v66, 0xb0, v132
	v_lshl_add_u64 v[32:33], v[130:131], 0, v[32:33]
	v_ashrrev_i32_e32 v67, 31, v66
	global_load_dwordx4 v[42:45], v[32:33], off nt
	global_load_dwordx4 v[46:49], v[32:33], off offset:64 nt
	global_load_dwordx4 v[50:53], v[32:33], off offset:512 nt
	global_load_dwordx4 v[54:57], v[32:33], off offset:576 nt
	v_lshlrev_b64 v[32:33], 12, v[66:67]
	v_lshl_add_u64 v[32:33], v[130:131], 0, v[32:33]
	global_load_dwordx4 v[58:61], v[32:33], off nt
	global_load_dwordx4 v[62:65], v[32:33], off offset:64 nt
	global_load_dwordx4 v[36:39], v[32:33], off offset:512 nt
	s_nop 0
	global_load_dwordx4 v[32:35], v[32:33], off offset:576 nt
	s_waitcnt vmcnt(0)
	v_pk_add_f32 v[30:31], v[30:31], v[44:45]
	v_pk_add_f32 v[28:29], v[28:29], v[42:43]
	v_pk_add_f32 v[26:27], v[26:27], v[48:49]
	v_pk_add_f32 v[14:15], v[14:15], v[60:61]
	v_pk_add_f32 v[12:13], v[12:13], v[58:59]
	v_cvt_pk_bf16_f32 v28, v28, v29
	v_cvt_pk_bf16_f32 v29, v30, v31
	v_lshlrev_b64 v[30:31], 11, v[40:41]
	v_cvt_pk_bf16_f32 v12, v12, v13
	v_cvt_pk_bf16_f32 v13, v14, v15
	v_lshlrev_b64 v[14:15], 11, v[66:67]
	v_lshl_add_u64 v[30:31], s[34:35], 0, v[30:31]
	v_pk_add_f32 v[24:25], v[24:25], v[46:47]
	v_pk_add_f32 v[22:23], v[22:23], v[52:53]
	v_pk_add_f32 v[20:21], v[20:21], v[50:51]
	v_pk_add_f32 v[18:19], v[18:19], v[56:57]
	v_pk_add_f32 v[16:17], v[16:17], v[54:55]
	v_lshl_add_u64 v[14:15], s[34:35], 0, v[14:15]
	v_pk_add_f32 v[10:11], v[10:11], v[64:65]
	v_pk_add_f32 v[8:9], v[8:9], v[62:63]
	v_pk_add_f32 v[6:7], v[6:7], v[38:39]
	v_pk_add_f32 v[4:5], v[4:5], v[36:37]
	v_pk_add_f32 v[2:3], v[2:3], v[34:35]
	v_pk_add_f32 v[0:1], v[0:1], v[32:33]
	v_lshl_add_u64 v[30:31], v[30:31], 0, v[124:125]
	v_cvt_pk_bf16_f32 v24, v24, v25
	v_cvt_pk_bf16_f32 v25, v26, v27
	v_cvt_pk_bf16_f32 v20, v20, v21
	v_cvt_pk_bf16_f32 v21, v22, v23
	v_cvt_pk_bf16_f32 v16, v16, v17
	v_cvt_pk_bf16_f32 v17, v18, v19
	v_lshl_add_u64 v[14:15], v[14:15], 0, v[124:125]
	v_cvt_pk_bf16_f32 v8, v8, v9
	v_cvt_pk_bf16_f32 v9, v10, v11
	v_cvt_pk_bf16_f32 v4, v4, v5
	v_cvt_pk_bf16_f32 v5, v6, v7
	v_cvt_pk_bf16_f32 v0, v0, v1
	v_cvt_pk_bf16_f32 v1, v2, v3
	global_store_dwordx2 v[30:31], v[28:29], off nt
	global_store_dwordx2 v[30:31], v[24:25], off offset:32 nt
	global_store_dwordx2 v[30:31], v[20:21], off offset:256 nt
	global_store_dwordx2 v[30:31], v[16:17], off offset:288 nt
	global_store_dwordx2 v[14:15], v[12:13], off nt
	global_store_dwordx2 v[14:15], v[8:9], off offset:32 nt
	global_store_dwordx2 v[14:15], v[4:5], off offset:256 nt
	global_store_dwordx2 v[14:15], v[0:1], off offset:288 nt
	s_cbranch_vccnz .LBB0_1085
	s_andn2_b64 vcc, exec, s[36:37]
	s_cbranch_vccnz .LBB0_1084
	s_barrier
	s_branch .LBB0_1084

.LBB0_1842:
	v_readlane_b32 s2, v252, 1
	v_readlane_b32 s3, v252, 2
	v_mbcnt_lo_u32_b32 v22, -1, 0
	v_mbcnt_hi_u32_b32 v22, -1, v22
	v_readlane_b32 s6, v252, 6
	v_readlane_b32 s7, v252, 7
	s_add_i32 s40, s6, s7
	s_add_u32 s6, s2, 0x344000
	s_addc_u32 s7, s3, 0
	s_add_u32 s10, s2, 0x384000
	s_addc_u32 s11, s3, 0
	s_add_u32 s44, s2, 0x1da00000
	s_addc_u32 s45, s3, 0
	s_add_u32 s31, s2, 0xb800000
	s_addc_u32 s33, s3, 0
	s_add_u32 s46, s2, 0x2400000
	s_addc_u32 s47, s3, 0
	s_lshl_b32 s18, s40, 1
	s_ashr_i32 s19, s18, 31
	s_lshl_b64 s[22:23], s[18:19], 2
	s_add_u32 s2, s6, s22
	s_addc_u32 s3, s7, s23
	s_add_u32 s22, s10, s22
	s_addc_u32 s23, s11, s23
	s_add_i32 s19, s18, 0x1000
	s_cmpk_lt_i32 s40, 0x7800
	s_cselect_b32 s18, s19, s18
	s_ashr_i32 s19, s18, 31
	s_lshl_b64 s[34:35], s[18:19], 2
	s_add_u32 s18, s6, s34
	s_addc_u32 s19, s7, s35
	global_load_dwordx2 v[0:1], v161, s[18:19] nt
	s_add_u32 s34, s10, s34
	s_addc_u32 s35, s11, s35
	s_ashr_i32 s41, s40, 31
	v_ashrrev_i32_e32 v23, 31, v22
	v_lshlrev_b64 v[26:27], 3, v[22:23]
	s_waitcnt vmcnt(0)
	v_readfirstlane_b32 s18, v0
	v_readfirstlane_b32 s19, v1
	global_load_dwordx2 v[2:3], v161, s[22:23] nt
	global_load_dwordx2 v[0:1], v161, s[34:35] nt
	global_load_dwordx2 v[4:5], v161, s[2:3] nt
	s_lshl_b64 s[22:23], s[40:41], 11
	s_add_u32 s22, s46, s22
	s_addc_u32 s23, s47, s23
	v_lshl_add_u64 v[18:19], s[22:23], 0, v[26:27]
	global_load_dwordx2 v[24:25], v[18:19], off nt
	s_mov_b32 s3, 0xffff
	s_waitcnt vmcnt(1)
	v_readfirstlane_b32 s22, v4
	s_ashr_i32 s23, s22, 31
	s_lshl_b64 s[34:35], s[22:23], 11
	s_add_u32 s34, s44, s34
	s_addc_u32 s35, s45, s35
	s_cmp_lt_i32 s22, 0x10000
	s_cselect_b64 s[36:37], -1, 0
	s_add_i32 s96, s22, 0xffff0000
	s_lshl_b64 s[58:59], s[96:97], 12
	s_add_u32 s22, s31, s58
	s_addc_u32 s23, s33, s59
	s_ashr_i32 s39, s38, 31
	s_add_u32 s54, s96, s38
	s_addc_u32 s55, 0, s39
	s_lshl_b64 s[42:43], s[54:55], 12
	s_add_u32 s48, s31, s42
	s_addc_u32 s49, s33, s43
	s_lshl_b64 s[74:75], s[38:39], 13
	s_add_u32 s63, s31, s74
	s_addc_u32 s77, s33, s75
	s_add_u32 s50, s63, s58
	s_addc_u32 s51, s77, s59
	s_lshl_b64 s[42:43], s[38:39], 1
	s_add_u32 s80, s54, s42
	s_addc_u32 s81, s55, s43
	s_lshl_b64 s[54:55], s[80:81], 12
	s_add_u32 s54, s31, s54
	s_addc_u32 s55, s33, s55
	s_add_u32 s78, s63, s74
	s_addc_u32 s79, s77, s75
	s_add_u32 s74, s78, s58
	s_addc_u32 s75, s79, s59
	s_add_u32 s58, s80, s42
	s_addc_u32 s59, s81, s43
	s_lshl_b64 s[80:81], s[58:59], 12
	s_add_u32 s90, s31, s80
	s_addc_u32 s91, s33, s81
	s_add_u32 s58, s58, s38
	s_addc_u32 s59, s59, s39
	s_lshl_b64 s[58:59], s[58:59], 12
	s_add_u32 s92, s31, s58
	v_readfirstlane_b32 s2, v5
	v_lshl_add_u64 v[20:21], s[34:35], 0, v[26:27]
	v_cmp_lt_i32_e64 s[34:35], s3, v5
	s_addc_u32 s93, s33, s59
	s_mov_b64 s[58:59], -1
	s_and_b64 vcc, exec, s[36:37]
	s_cbranch_vccz .LBB0_1844
	global_load_dwordx2 v[6:7], v[20:21], off nt
	s_mov_b64 s[58:59], 0
.LBB0_1844:
	v_lshlrev_b64 v[4:5], 4, v[22:23]
	s_andn2_b64 vcc, exec, s[58:59]
	v_lshl_add_u64 v[38:39], s[22:23], 0, v[4:5]
	v_lshl_add_u64 v[40:41], s[48:49], 0, v[4:5]
	v_lshl_add_u64 v[36:37], s[50:51], 0, v[4:5]
	v_lshl_add_u64 v[34:35], s[54:55], 0, v[4:5]
	v_lshl_add_u64 v[32:33], s[74:75], 0, v[4:5]
	v_lshl_add_u64 v[30:31], s[90:91], 0, v[4:5]
	v_lshl_add_u64 v[28:29], s[92:93], 0, v[4:5]
	s_cbranch_vccnz .LBB0_1846
	global_load_dwordx4 v[6:9], v[38:39], off nt
	global_load_dwordx4 v[10:13], v[40:41], off nt
	s_waitcnt vmcnt(0)
	v_pk_add_f32 v[12:13], v[8:9], v[12:13]
	v_pk_add_f32 v[10:11], v[6:7], v[10:11]
	global_load_dwordx4 v[6:9], v[36:37], off nt
	s_waitcnt vmcnt(0)
	v_pk_add_f32 v[12:13], v[12:13], v[8:9]
	v_pk_add_f32 v[10:11], v[10:11], v[6:7]
	global_load_dwordx4 v[6:9], v[34:35], off nt
	s_waitcnt vmcnt(0)
	v_pk_add_f32 v[12:13], v[12:13], v[8:9]
	v_pk_add_f32 v[10:11], v[10:11], v[6:7]
	global_load_dwordx4 v[6:9], v[32:33], off nt
	s_waitcnt vmcnt(0)
	v_pk_add_f32 v[12:13], v[12:13], v[8:9]
	v_pk_add_f32 v[10:11], v[10:11], v[6:7]
	global_load_dwordx4 v[6:9], v[30:31], off nt
	s_waitcnt vmcnt(0)
	v_pk_add_f32 v[12:13], v[12:13], v[8:9]
	v_pk_add_f32 v[10:11], v[10:11], v[6:7]
	global_load_dwordx4 v[6:9], v[28:29], off nt
	s_waitcnt vmcnt(0)
	v_pk_add_f32 v[8:9], v[12:13], v[8:9]
	v_pk_add_f32 v[6:7], v[10:11], v[6:7]
	v_pk_mul_f32 v[8:9], v[8:9], s[30:31] op_sel_hi:[1,0]
	v_pk_mul_f32 v[6:7], v[6:7], s[30:31] op_sel_hi:[1,0]
	s_nop 0
	v_cvt_pk_bf16_f32 v6, v6, v7
	v_cvt_pk_bf16_f32 v7, v8, v9
.LBB0_1846:
	s_ashr_i32 s3, s2, 31
	s_lshl_b64 s[22:23], s[2:3], 11
	s_add_u32 s22, s44, s22
	s_addc_u32 s23, s45, s23
	s_add_i32 s96, s2, 0xffff0000
	s_lshl_b64 s[2:3], s[96:97], 12
	v_lshl_add_u64 v[44:45], v[22:23], 3, s[22:23]
	s_add_u32 s22, s31, s2
	s_addc_u32 s23, s33, s3
	s_add_u32 s54, s96, s38
	s_addc_u32 s55, 0, s39
	s_lshl_b64 s[48:49], s[54:55], 12
	s_add_u32 s48, s31, s48
	s_addc_u32 s49, s33, s49
	s_add_u32 s50, s63, s2
	s_addc_u32 s51, s77, s3
	s_add_u32 s74, s54, s42
	s_addc_u32 s75, s55, s43
	s_lshl_b64 s[54:55], s[74:75], 12
	s_add_u32 s54, s31, s54
	s_addc_u32 s55, s33, s55
	s_add_u32 s58, s78, s2
	s_addc_u32 s59, s79, s3
	s_add_u32 s2, s74, s42
	s_addc_u32 s3, s75, s43
	s_lshl_b64 s[74:75], s[2:3], 12
	s_add_u32 s74, s31, s74
	s_addc_u32 s75, s33, s75
	s_add_u32 s2, s2, s38
	s_addc_u32 s3, s3, s39
	s_lshl_b64 s[2:3], s[2:3], 12
	s_add_u32 s90, s31, s2
	s_addc_u32 s91, s33, s3
	s_xor_b64 s[2:3], s[34:35], -1
	s_mov_b64 s[92:93], -1
	s_and_b64 vcc, exec, s[2:3]
	s_cbranch_vccz .LBB0_1848
	global_load_dwordx2 v[8:9], v[44:45], off nt
	s_mov_b64 s[92:93], 0
.LBB0_1848:
	s_andn2_b64 vcc, exec, s[92:93]
	v_lshl_add_u64 v[56:57], s[22:23], 0, v[4:5]
	v_lshl_add_u64 v[58:59], s[48:49], 0, v[4:5]
	v_lshl_add_u64 v[52:53], s[50:51], 0, v[4:5]
	v_lshl_add_u64 v[50:51], s[54:55], 0, v[4:5]
	v_lshl_add_u64 v[48:49], s[58:59], 0, v[4:5]
	v_lshl_add_u64 v[46:47], s[74:75], 0, v[4:5]
	v_lshl_add_u64 v[42:43], s[90:91], 0, v[4:5]
	s_cbranch_vccnz .LBB0_1850
	global_load_dwordx4 v[8:11], v[56:57], off nt
	global_load_dwordx4 v[12:15], v[58:59], off nt
	s_waitcnt vmcnt(0)
	v_pk_add_f32 v[14:15], v[10:11], v[14:15]
	v_pk_add_f32 v[12:13], v[8:9], v[12:13]
	global_load_dwordx4 v[8:11], v[52:53], off nt
	s_waitcnt vmcnt(0)
	v_pk_add_f32 v[14:15], v[14:15], v[10:11]
	v_pk_add_f32 v[12:13], v[12:13], v[8:9]
	global_load_dwordx4 v[8:11], v[50:51], off nt
	s_waitcnt vmcnt(0)
	v_pk_add_f32 v[14:15], v[14:15], v[10:11]
	v_pk_add_f32 v[12:13], v[12:13], v[8:9]
	global_load_dwordx4 v[8:11], v[48:49], off nt
	s_waitcnt vmcnt(0)
	v_pk_add_f32 v[14:15], v[14:15], v[10:11]
	v_pk_add_f32 v[12:13], v[12:13], v[8:9]
	global_load_dwordx4 v[8:11], v[46:47], off nt
	s_waitcnt vmcnt(0)
	v_pk_add_f32 v[14:15], v[14:15], v[10:11]
	v_pk_add_f32 v[12:13], v[12:13], v[8:9]
	global_load_dwordx4 v[8:11], v[42:43], off nt
	s_waitcnt vmcnt(0)
	v_pk_add_f32 v[10:11], v[14:15], v[10:11]
	v_pk_add_f32 v[8:9], v[12:13], v[8:9]
	v_pk_mul_f32 v[10:11], v[10:11], s[30:31] op_sel_hi:[1,0]
	v_pk_mul_f32 v[8:9], v[8:9], s[30:31] op_sel_hi:[1,0]
	s_nop 0
	v_cvt_pk_bf16_f32 v8, v8, v9
	v_cvt_pk_bf16_f32 v9, v10, v11
.LBB0_1850:
	global_load_dwordx2 v[54:55], v[18:19], off offset:512 nt
	v_cndmask_b32_e64 v10, 0, 1, s[36:37]
	v_cmp_ne_u32_e64 s[34:35], 1, v10
	s_andn2_b64 vcc, exec, s[36:37]
	s_mov_b64 s[22:23], -1
	s_cbranch_vccnz .LBB0_1852
	global_load_dwordx2 v[10:11], v[20:21], off offset:512 nt
	s_mov_b64 s[22:23], 0
.LBB0_1852:
	s_andn2_b64 vcc, exec, s[22:23]
	s_cbranch_vccnz .LBB0_1854
	global_load_dwordx4 v[10:13], v[38:39], off offset:1024 nt
	global_load_dwordx4 v[14:17], v[40:41], off offset:1024 nt
	s_waitcnt vmcnt(0)
	v_pk_add_f32 v[16:17], v[12:13], v[16:17]
	v_pk_add_f32 v[14:15], v[10:11], v[14:15]
	global_load_dwordx4 v[10:13], v[36:37], off offset:1024 nt
	s_waitcnt vmcnt(0)
	v_pk_add_f32 v[16:17], v[16:17], v[12:13]
	v_pk_add_f32 v[14:15], v[14:15], v[10:11]
	global_load_dwordx4 v[10:13], v[34:35], off offset:1024 nt
	s_waitcnt vmcnt(0)
	v_pk_add_f32 v[16:17], v[16:17], v[12:13]
	v_pk_add_f32 v[14:15], v[14:15], v[10:11]
	global_load_dwordx4 v[10:13], v[32:33], off offset:1024 nt
	s_waitcnt vmcnt(0)
	v_pk_add_f32 v[16:17], v[16:17], v[12:13]
	v_pk_add_f32 v[14:15], v[14:15], v[10:11]
	global_load_dwordx4 v[10:13], v[30:31], off offset:1024 nt
	s_waitcnt vmcnt(0)
	v_pk_add_f32 v[16:17], v[16:17], v[12:13]
	v_pk_add_f32 v[14:15], v[14:15], v[10:11]
	global_load_dwordx4 v[10:13], v[28:29], off offset:1024 nt
	s_waitcnt vmcnt(0)
	v_pk_add_f32 v[12:13], v[16:17], v[12:13]
	v_pk_add_f32 v[10:11], v[14:15], v[10:11]
	v_pk_mul_f32 v[12:13], v[12:13], s[30:31] op_sel_hi:[1,0]
	v_pk_mul_f32 v[10:11], v[10:11], s[30:31] op_sel_hi:[1,0]
	s_nop 0
	v_cvt_pk_bf16_f32 v10, v10, v11
	v_cvt_pk_bf16_f32 v11, v12, v13
.LBB0_1854:
	v_cndmask_b32_e64 v12, 0, 1, s[2:3]
	v_cmp_ne_u32_e64 s[36:37], 1, v12
	s_andn2_b64 vcc, exec, s[2:3]
	s_mov_b64 s[2:3], -1
	s_cbranch_vccnz .LBB0_1856
	global_load_dwordx2 v[12:13], v[44:45], off offset:512 nt
	s_cbranch_execnz .LBB0_1858
	s_branch .LBB0_1857

.LBB0_1857:
	global_load_dwordx4 v[12:15], v[56:57], off offset:1024 nt
	global_load_dwordx4 v[60:63], v[58:59], off offset:1024 nt
	s_waitcnt vmcnt(0)
	v_pk_add_f32 v[16:17], v[14:15], v[62:63]
	v_pk_add_f32 v[60:61], v[12:13], v[60:61]
	global_load_dwordx4 v[12:15], v[52:53], off offset:1024 nt
	s_waitcnt vmcnt(0)
	v_pk_add_f32 v[16:17], v[16:17], v[14:15]
	v_pk_add_f32 v[60:61], v[60:61], v[12:13]
	global_load_dwordx4 v[12:15], v[50:51], off offset:1024 nt
	s_waitcnt vmcnt(0)
	v_pk_add_f32 v[16:17], v[16:17], v[14:15]
	v_pk_add_f32 v[60:61], v[60:61], v[12:13]
	global_load_dwordx4 v[12:15], v[48:49], off offset:1024 nt
	s_waitcnt vmcnt(0)
	v_pk_add_f32 v[16:17], v[16:17], v[14:15]
	v_pk_add_f32 v[60:61], v[60:61], v[12:13]
	global_load_dwordx4 v[12:15], v[46:47], off offset:1024 nt
	s_waitcnt vmcnt(0)
	v_pk_add_f32 v[16:17], v[16:17], v[14:15]
	v_pk_add_f32 v[60:61], v[60:61], v[12:13]
	global_load_dwordx4 v[12:15], v[42:43], off offset:1024 nt
	s_waitcnt vmcnt(0)
	v_pk_add_f32 v[14:15], v[16:17], v[14:15]
	v_pk_add_f32 v[12:13], v[60:61], v[12:13]
	v_pk_mul_f32 v[14:15], v[14:15], s[30:31] op_sel_hi:[1,0]
	v_pk_mul_f32 v[12:13], v[12:13], s[30:31] op_sel_hi:[1,0]
	s_nop 0
	v_cvt_pk_bf16_f32 v12, v12, v13
	v_cvt_pk_bf16_f32 v13, v14, v15
.LBB0_1858:
	global_load_dwordx2 v[60:61], v[18:19], off offset:1024 nt
	s_and_b64 vcc, exec, s[34:35]
	s_mov_b64 s[2:3], -1
	s_cbranch_vccnz .LBB0_1862
	global_load_dwordx2 v[14:15], v[20:21], off offset:1024 nt
	s_cbranch_execz .LBB0_1863

.LBB0_1861:
	global_load_dwordx2 v[16:17], v[44:45], off offset:1024 nt
	s_cbranch_execnz .LBB0_1866
	s_branch .LBB0_1865

.LBB0_1863:
	global_load_dwordx4 v[14:17], v[38:39], off offset:2048 nt
	global_load_dwordx4 v[62:65], v[40:41], off offset:2048 nt
	s_waitcnt vmcnt(0)
	v_pk_add_f32 v[64:65], v[16:17], v[64:65]
	v_pk_add_f32 v[62:63], v[14:15], v[62:63]
	global_load_dwordx4 v[14:17], v[36:37], off offset:2048 nt
	s_waitcnt vmcnt(0)
	v_pk_add_f32 v[64:65], v[64:65], v[16:17]
	v_pk_add_f32 v[62:63], v[62:63], v[14:15]
	global_load_dwordx4 v[14:17], v[34:35], off offset:2048 nt
	s_waitcnt vmcnt(0)
	v_pk_add_f32 v[64:65], v[64:65], v[16:17]
	v_pk_add_f32 v[62:63], v[62:63], v[14:15]
	global_load_dwordx4 v[14:17], v[32:33], off offset:2048 nt
	s_waitcnt vmcnt(0)
	v_pk_add_f32 v[64:65], v[64:65], v[16:17]
	v_pk_add_f32 v[62:63], v[62:63], v[14:15]
	global_load_dwordx4 v[14:17], v[30:31], off offset:2048 nt
	s_waitcnt vmcnt(0)
	v_pk_add_f32 v[64:65], v[64:65], v[16:17]
	v_pk_add_f32 v[62:63], v[62:63], v[14:15]
	global_load_dwordx4 v[14:17], v[28:29], off offset:2048 nt
	s_waitcnt vmcnt(0)
	v_pk_add_f32 v[16:17], v[64:65], v[16:17]
	v_pk_add_f32 v[14:15], v[62:63], v[14:15]
	v_pk_mul_f32 v[16:17], v[16:17], s[30:31] op_sel_hi:[1,0]
	v_pk_mul_f32 v[14:15], v[14:15], s[30:31] op_sel_hi:[1,0]
	s_nop 0
	v_cvt_pk_bf16_f32 v14, v14, v15
	v_cvt_pk_bf16_f32 v15, v16, v17
	s_and_b64 vcc, exec, s[36:37]
	s_mov_b64 s[2:3], -1
	s_cbranch_vccz .LBB0_1861

.LBB0_1865:
	global_load_dwordx4 v[62:65], v[56:57], off offset:2048 nt
	global_load_dwordx4 v[66:69], v[58:59], off offset:2048 nt
	s_waitcnt vmcnt(0)
	v_pk_add_f32 v[16:17], v[64:65], v[68:69]
	v_pk_add_f32 v[66:67], v[62:63], v[66:67]
	global_load_dwordx4 v[62:65], v[52:53], off offset:2048 nt
	s_waitcnt vmcnt(0)
	v_pk_add_f32 v[16:17], v[16:17], v[64:65]
	v_pk_add_f32 v[66:67], v[66:67], v[62:63]
	global_load_dwordx4 v[62:65], v[50:51], off offset:2048 nt
	s_waitcnt vmcnt(0)
	v_pk_add_f32 v[16:17], v[16:17], v[64:65]
	v_pk_add_f32 v[66:67], v[66:67], v[62:63]
	global_load_dwordx4 v[62:65], v[48:49], off offset:2048 nt
	s_waitcnt vmcnt(0)
	v_pk_add_f32 v[16:17], v[16:17], v[64:65]
	v_pk_add_f32 v[66:67], v[66:67], v[62:63]
	global_load_dwordx4 v[62:65], v[46:47], off offset:2048 nt
	s_waitcnt vmcnt(0)
	v_pk_add_f32 v[16:17], v[16:17], v[64:65]
	v_pk_add_f32 v[66:67], v[66:67], v[62:63]
	global_load_dwordx4 v[62:65], v[42:43], off offset:2048 nt
	s_waitcnt vmcnt(0)
	v_pk_add_f32 v[64:65], v[16:17], v[64:65]
	v_pk_add_f32 v[16:17], v[66:67], v[62:63]
	v_pk_mul_f32 v[62:63], v[64:65], s[30:31] op_sel_hi:[1,0]
	v_pk_mul_f32 v[16:17], v[16:17], s[30:31] op_sel_hi:[1,0]
	s_nop 0
	v_cvt_pk_bf16_f32 v16, v16, v17
	v_cvt_pk_bf16_f32 v17, v62, v63
.LBB0_1866:
	global_load_dwordx2 v[62:63], v[18:19], off offset:1536 nt
	s_and_b64 vcc, exec, s[34:35]
	s_mov_b64 s[2:3], -1
	s_cbranch_vccnz .LBB0_1871
	global_load_dwordx2 v[18:19], v[20:21], off offset:1536 nt
	s_cbranch_execz .LBB0_1872

.LBB0_1869:
	global_load_dwordx2 v[20:21], v[44:45], off offset:1536 nt
	s_cbranch_execz .LBB0_1874

.LBB0_1872:
	global_load_dwordx4 v[18:21], v[38:39], off offset:3072 nt
	s_nop 0
	global_load_dwordx4 v[38:41], v[40:41], off offset:3072 nt
	s_waitcnt vmcnt(0)
	v_pk_add_f32 v[40:41], v[20:21], v[40:41]
	v_pk_add_f32 v[38:39], v[18:19], v[38:39]
	global_load_dwordx4 v[18:21], v[36:37], off offset:3072 nt
	s_waitcnt vmcnt(0)
	v_pk_add_f32 v[36:37], v[40:41], v[20:21]
	v_pk_add_f32 v[38:39], v[38:39], v[18:19]
	global_load_dwordx4 v[18:21], v[34:35], off offset:3072 nt
	s_waitcnt vmcnt(0)
	v_pk_add_f32 v[34:35], v[36:37], v[20:21]
	v_pk_add_f32 v[36:37], v[38:39], v[18:19]
	global_load_dwordx4 v[18:21], v[32:33], off offset:3072 nt
	s_waitcnt vmcnt(0)
	v_pk_add_f32 v[32:33], v[34:35], v[20:21]
	v_pk_add_f32 v[34:35], v[36:37], v[18:19]
	global_load_dwordx4 v[18:21], v[30:31], off offset:3072 nt
	s_waitcnt vmcnt(0)
	v_pk_add_f32 v[30:31], v[32:33], v[20:21]
	v_pk_add_f32 v[32:33], v[34:35], v[18:19]
	global_load_dwordx4 v[18:21], v[28:29], off offset:3072 nt
	s_waitcnt vmcnt(0)
	v_pk_add_f32 v[20:21], v[30:31], v[20:21]
	v_pk_add_f32 v[18:19], v[32:33], v[18:19]
	v_pk_mul_f32 v[20:21], v[20:21], s[30:31] op_sel_hi:[1,0]
	v_pk_mul_f32 v[18:19], v[18:19], s[30:31] op_sel_hi:[1,0]
	s_nop 0
	v_cvt_pk_bf16_f32 v18, v18, v19
	v_cvt_pk_bf16_f32 v19, v20, v21
	s_and_b64 vcc, exec, s[36:37]
	s_mov_b64 s[2:3], -1
	s_cbranch_vccz .LBB0_1869

.LBB0_1874:
	global_load_dwordx4 v[28:31], v[56:57], off offset:3072 nt
	global_load_dwordx4 v[32:35], v[58:59], off offset:3072 nt
	s_waitcnt vmcnt(0)
	v_pk_add_f32 v[20:21], v[30:31], v[34:35]
	v_pk_add_f32 v[32:33], v[28:29], v[32:33]
	global_load_dwordx4 v[28:31], v[52:53], off offset:3072 nt
	s_waitcnt vmcnt(0)
	v_pk_add_f32 v[20:21], v[20:21], v[30:31]
	v_pk_add_f32 v[32:33], v[32:33], v[28:29]
	global_load_dwordx4 v[28:31], v[50:51], off offset:3072 nt
	s_waitcnt vmcnt(0)
	v_pk_add_f32 v[20:21], v[20:21], v[30:31]
	v_pk_add_f32 v[32:33], v[32:33], v[28:29]
	global_load_dwordx4 v[28:31], v[48:49], off offset:3072 nt
	s_waitcnt vmcnt(0)
	v_pk_add_f32 v[20:21], v[20:21], v[30:31]
	v_pk_add_f32 v[32:33], v[32:33], v[28:29]
	global_load_dwordx4 v[28:31], v[46:47], off offset:3072 nt
	s_waitcnt vmcnt(0)
	v_pk_add_f32 v[20:21], v[20:21], v[30:31]
	v_pk_add_f32 v[32:33], v[32:33], v[28:29]
	global_load_dwordx4 v[28:31], v[42:43], off offset:3072 nt
	s_waitcnt vmcnt(0)
	v_pk_add_f32 v[30:31], v[20:21], v[30:31]
	v_pk_add_f32 v[20:21], v[32:33], v[28:29]
	v_pk_mul_f32 v[28:29], v[30:31], s[30:31] op_sel_hi:[1,0]
	v_pk_mul_f32 v[20:21], v[20:21], s[30:31] op_sel_hi:[1,0]
	s_nop 0
	v_cvt_pk_bf16_f32 v20, v20, v21
	v_cvt_pk_bf16_f32 v21, v28, v29
	s_cmp_lt_i32 s40, 0x8000
	s_cbranch_scc1 .LBB0_1875
	s_getpc_b64 s[98:99]

.LBB0_1877:
	s_add_i32 s2, s41, 0x1000
	s_cmpk_lt_i32 s41, 0x7000
	s_cselect_b32 s2, s2, s40
	s_lshl_b32 s2, s2, 1
	s_ashr_i32 s3, s2, 31
	s_lshl_b64 s[2:3], s[2:3], 2
	s_add_u32 s22, s6, s2
	s_addc_u32 s23, s7, s3
	global_load_dwordx2 v[44:45], v161, s[22:23] nt
	s_add_u32 s2, s10, s2
	s_mov_b32 s34, s41
	s_addc_u32 s3, s11, s3
	s_addk_i32 s41, 0x800
	s_cmpk_gt_i32 s34, 0x77ff
	s_cselect_b64 s[46:47], -1, 0
	s_cmpk_lt_i32 s34, 0x7800
	s_mov_b32 s22, s18
	s_waitcnt vmcnt(0)
	v_readfirstlane_b32 s44, v44
	v_readfirstlane_b32 s45, v45
	global_load_dwordx2 v[44:45], v161, s[2:3] nt
	s_cselect_b32 s2, s41, s40
	s_ashr_i32 s3, s2, 31
	s_lshl_b64 s[2:3], s[2:3], 11
	v_lshl_add_u64 v[52:53], v[26:27], 0, s[2:3]
	global_load_dwordx2 v[46:47], v[52:53], off nt
	s_ashr_i32 s23, s18, 31
	s_lshl_b64 s[22:23], s[22:23], 11
	s_cmp_lt_i32 s18, 0x10000
	s_cselect_b64 s[2:3], -1, 0
	s_add_i32 s96, s18, 0xffff0000
	s_lshl_b64 s[50:51], s[96:97], 12
	v_lshl_add_u64 v[50:51], v[24:25], 0, s[22:23]
	s_add_u32 s22, s31, s50
	s_addc_u32 s23, s33, s51
	s_add_u32 s48, s96, s38
	s_addc_u32 s49, 0, s39
	s_lshl_b64 s[34:35], s[48:49], 12
	s_add_u32 s34, s31, s34
	s_addc_u32 s35, s33, s35
	s_add_u32 s36, s63, s50
	s_addc_u32 s37, s77, s51
	s_add_u32 s54, s48, s42
	s_addc_u32 s55, s49, s43
	s_lshl_b64 s[48:49], s[54:55], 12
	s_add_u32 s48, s31, s48
	s_addc_u32 s49, s33, s49
	s_add_u32 s50, s78, s50
	s_addc_u32 s51, s79, s51
	s_add_u32 s58, s54, s42
	s_addc_u32 s59, s55, s43
	s_lshl_b64 s[54:55], s[58:59], 12
	s_add_u32 s54, s31, s54
	s_addc_u32 s55, s33, s55
	s_add_u32 s58, s58, s38
	s_addc_u32 s59, s59, s39
	s_lshl_b64 s[58:59], s[58:59], 12
	s_add_u32 s74, s31, s58
	s_addc_u32 s75, s33, s59
	s_mov_b64 s[58:59], -1
	s_and_b64 vcc, exec, s[2:3]
	s_cbranch_vccz .LBB0_1879
	global_load_dwordx2 v[48:49], v[50:51], off nt
	s_mov_b64 s[58:59], 0
.LBB0_1879:
	s_andn2_b64 vcc, exec, s[58:59]
	v_lshl_add_u64 v[66:67], s[22:23], 0, v[4:5]
	v_lshl_add_u64 v[68:69], s[34:35], 0, v[4:5]
	v_lshl_add_u64 v[64:65], s[36:37], 0, v[4:5]
	v_lshl_add_u64 v[62:63], s[48:49], 0, v[4:5]
	v_lshl_add_u64 v[60:61], s[50:51], 0, v[4:5]
	v_lshl_add_u64 v[58:59], s[54:55], 0, v[4:5]
	v_lshl_add_u64 v[56:57], s[74:75], 0, v[4:5]
	s_cbranch_vccnz .LBB0_1881
	global_load_dwordx4 v[70:73], v[66:67], off nt
	global_load_dwordx4 v[74:77], v[68:69], off nt
	s_waitcnt vmcnt(0)
	v_pk_add_f32 v[48:49], v[72:73], v[76:77]
	v_pk_add_f32 v[54:55], v[70:71], v[74:75]
	global_load_dwordx4 v[70:73], v[64:65], off nt
	s_waitcnt vmcnt(0)
	v_pk_add_f32 v[48:49], v[48:49], v[72:73]
	v_pk_add_f32 v[54:55], v[54:55], v[70:71]
	global_load_dwordx4 v[70:73], v[62:63], off nt
	s_waitcnt vmcnt(0)
	v_pk_add_f32 v[48:49], v[48:49], v[72:73]
	v_pk_add_f32 v[54:55], v[54:55], v[70:71]
	global_load_dwordx4 v[70:73], v[60:61], off nt
	s_waitcnt vmcnt(0)
	v_pk_add_f32 v[48:49], v[48:49], v[72:73]
	v_pk_add_f32 v[54:55], v[54:55], v[70:71]
	global_load_dwordx4 v[70:73], v[58:59], off nt
	s_waitcnt vmcnt(0)
	v_pk_add_f32 v[48:49], v[48:49], v[72:73]
	v_pk_add_f32 v[54:55], v[54:55], v[70:71]
	global_load_dwordx4 v[70:73], v[56:57], off nt
	s_waitcnt vmcnt(0)
	v_pk_add_f32 v[72:73], v[48:49], v[72:73]
	v_pk_add_f32 v[48:49], v[54:55], v[70:71]
	v_pk_mul_f32 v[54:55], v[72:73], s[30:31] op_sel_hi:[1,0]
	v_pk_mul_f32 v[48:49], v[48:49], s[30:31] op_sel_hi:[1,0]
	s_nop 0
	v_cvt_pk_bf16_f32 v48, v48, v49
	v_cvt_pk_bf16_f32 v49, v54, v55
.LBB0_1881:
	s_ashr_i32 s23, s19, 31
	s_mov_b32 s22, s19
	s_lshl_b64 s[22:23], s[22:23], 11
	s_cmp_lt_i32 s19, 0x10000
	v_lshl_add_u64 v[72:73], v[24:25], 0, s[22:23]
	s_cselect_b64 s[22:23], -1, 0
	s_add_i32 s96, s19, 0xffff0000
	s_lshl_b64 s[50:51], s[96:97], 12
	s_add_u32 s18, s31, s50
	s_addc_u32 s19, s33, s51
	s_add_u32 s48, s96, s38
	s_addc_u32 s49, 0, s39
	s_lshl_b64 s[34:35], s[48:49], 12
	s_add_u32 s34, s31, s34
	s_addc_u32 s35, s33, s35
	s_add_u32 s36, s63, s50
	s_addc_u32 s37, s77, s51
	s_add_u32 s54, s48, s42
	s_addc_u32 s55, s49, s43
	s_lshl_b64 s[48:49], s[54:55], 12
	s_add_u32 s48, s31, s48
	s_addc_u32 s49, s33, s49
	s_add_u32 s50, s78, s50
	s_addc_u32 s51, s79, s51
	s_add_u32 s58, s54, s42
	s_addc_u32 s59, s55, s43
	s_lshl_b64 s[54:55], s[58:59], 12
	s_add_u32 s54, s31, s54
	s_addc_u32 s55, s33, s55
	s_add_u32 s58, s58, s38
	s_addc_u32 s59, s59, s39
	s_lshl_b64 s[58:59], s[58:59], 12
	s_add_u32 s58, s31, s58
	s_addc_u32 s59, s33, s59
	s_mov_b64 s[74:75], -1
	s_and_b64 vcc, exec, s[22:23]
	s_cbranch_vccz .LBB0_1883
	global_load_dwordx2 v[54:55], v[72:73], off nt
	s_mov_b64 s[74:75], 0
.LBB0_1883:
	s_andn2_b64 vcc, exec, s[74:75]
	v_lshl_add_u64 v[84:85], s[18:19], 0, v[4:5]
	v_lshl_add_u64 v[86:87], s[34:35], 0, v[4:5]
	v_lshl_add_u64 v[82:83], s[36:37], 0, v[4:5]
	v_lshl_add_u64 v[80:81], s[48:49], 0, v[4:5]
	v_lshl_add_u64 v[76:77], s[50:51], 0, v[4:5]
	v_lshl_add_u64 v[74:75], s[54:55], 0, v[4:5]
	v_lshl_add_u64 v[70:71], s[58:59], 0, v[4:5]
	s_cbranch_vccnz .LBB0_1885
	global_load_dwordx4 v[88:91], v[84:85], off nt
	global_load_dwordx4 v[92:95], v[86:87], off nt
	s_waitcnt vmcnt(0)
	v_pk_add_f32 v[54:55], v[90:91], v[94:95]
	v_pk_add_f32 v[78:79], v[88:89], v[92:93]
	global_load_dwordx4 v[88:91], v[82:83], off nt
	s_waitcnt vmcnt(0)
	v_pk_add_f32 v[54:55], v[54:55], v[90:91]
	v_pk_add_f32 v[78:79], v[78:79], v[88:89]
	global_load_dwordx4 v[88:91], v[80:81], off nt
	s_waitcnt vmcnt(0)
	v_pk_add_f32 v[54:55], v[54:55], v[90:91]
	v_pk_add_f32 v[78:79], v[78:79], v[88:89]
	global_load_dwordx4 v[88:91], v[76:77], off nt
	s_waitcnt vmcnt(0)
	v_pk_add_f32 v[54:55], v[54:55], v[90:91]
	v_pk_add_f32 v[78:79], v[78:79], v[88:89]
	global_load_dwordx4 v[88:91], v[74:75], off nt
	s_waitcnt vmcnt(0)
	v_pk_add_f32 v[54:55], v[54:55], v[90:91]
	v_pk_add_f32 v[78:79], v[78:79], v[88:89]
	global_load_dwordx4 v[88:91], v[70:71], off nt
	s_waitcnt vmcnt(0)
	v_pk_add_f32 v[90:91], v[54:55], v[90:91]
	v_pk_add_f32 v[54:55], v[78:79], v[88:89]
	v_pk_mul_f32 v[78:79], v[90:91], s[30:31] op_sel_hi:[1,0]
	v_pk_mul_f32 v[54:55], v[54:55], s[30:31] op_sel_hi:[1,0]
	s_nop 0
	v_cvt_pk_bf16_f32 v54, v54, v55
	v_cvt_pk_bf16_f32 v55, v78, v79
.LBB0_1885:
	global_load_dwordx2 v[88:89], v[52:53], off offset:512 nt
	v_cndmask_b32_e64 v78, 0, 1, s[2:3]
	v_cmp_ne_u32_e64 s[34:35], 1, v78
	s_andn2_b64 vcc, exec, s[2:3]
	s_mov_b64 s[2:3], -1
	s_cbranch_vccnz .LBB0_1887
	global_load_dwordx2 v[78:79], v[50:51], off offset:512 nt
	s_mov_b64 s[2:3], 0
.LBB0_1887:
	s_andn2_b64 vcc, exec, s[2:3]
	s_cbranch_vccnz .LBB0_1889
	global_load_dwordx4 v[90:93], v[66:67], off offset:1024 nt
	global_load_dwordx4 v[94:97], v[68:69], off offset:1024 nt
	s_waitcnt vmcnt(0)
	v_pk_add_f32 v[78:79], v[92:93], v[96:97]
	v_pk_add_f32 v[94:95], v[90:91], v[94:95]
	global_load_dwordx4 v[90:93], v[64:65], off offset:1024 nt
	s_waitcnt vmcnt(0)
	v_pk_add_f32 v[78:79], v[78:79], v[92:93]
	v_pk_add_f32 v[94:95], v[94:95], v[90:91]
	global_load_dwordx4 v[90:93], v[62:63], off offset:1024 nt
	s_waitcnt vmcnt(0)
	v_pk_add_f32 v[78:79], v[78:79], v[92:93]
	v_pk_add_f32 v[94:95], v[94:95], v[90:91]
	global_load_dwordx4 v[90:93], v[60:61], off offset:1024 nt
	s_waitcnt vmcnt(0)
	v_pk_add_f32 v[78:79], v[78:79], v[92:93]
	v_pk_add_f32 v[94:95], v[94:95], v[90:91]
	global_load_dwordx4 v[90:93], v[58:59], off offset:1024 nt
	s_waitcnt vmcnt(0)
	v_pk_add_f32 v[78:79], v[78:79], v[92:93]
	v_pk_add_f32 v[94:95], v[94:95], v[90:91]
	global_load_dwordx4 v[90:93], v[56:57], off offset:1024 nt
	s_waitcnt vmcnt(0)
	v_pk_add_f32 v[92:93], v[78:79], v[92:93]
	v_pk_add_f32 v[78:79], v[94:95], v[90:91]
	v_pk_mul_f32 v[90:91], v[92:93], s[30:31] op_sel_hi:[1,0]
	v_pk_mul_f32 v[78:79], v[78:79], s[30:31] op_sel_hi:[1,0]
	s_nop 0
	v_cvt_pk_bf16_f32 v78, v78, v79
	v_cvt_pk_bf16_f32 v79, v90, v91
.LBB0_1889:
	v_cndmask_b32_e64 v90, 0, 1, s[22:23]
	v_cmp_ne_u32_e64 s[36:37], 1, v90
	s_andn2_b64 vcc, exec, s[22:23]
	s_mov_b64 s[2:3], -1
	s_cbranch_vccnz .LBB0_1891
	global_load_dwordx2 v[90:91], v[72:73], off offset:512 nt
	s_cbranch_execnz .LBB0_1893
	s_branch .LBB0_1892

.LBB0_1892:
	global_load_dwordx4 v[90:93], v[84:85], off offset:1024 nt
	global_load_dwordx4 v[94:97], v[86:87], off offset:1024 nt
	s_waitcnt vmcnt(0)
	v_pk_add_f32 v[96:97], v[92:93], v[96:97]
	v_pk_add_f32 v[94:95], v[90:91], v[94:95]
	global_load_dwordx4 v[90:93], v[82:83], off offset:1024 nt
	s_waitcnt vmcnt(0)
	v_pk_add_f32 v[96:97], v[96:97], v[92:93]
	v_pk_add_f32 v[94:95], v[94:95], v[90:91]
	global_load_dwordx4 v[90:93], v[80:81], off offset:1024 nt
	s_waitcnt vmcnt(0)
	v_pk_add_f32 v[96:97], v[96:97], v[92:93]
	v_pk_add_f32 v[94:95], v[94:95], v[90:91]
	global_load_dwordx4 v[90:93], v[76:77], off offset:1024 nt
	s_waitcnt vmcnt(0)
	v_pk_add_f32 v[96:97], v[96:97], v[92:93]
	v_pk_add_f32 v[94:95], v[94:95], v[90:91]
	global_load_dwordx4 v[90:93], v[74:75], off offset:1024 nt
	s_waitcnt vmcnt(0)
	v_pk_add_f32 v[96:97], v[96:97], v[92:93]
	v_pk_add_f32 v[94:95], v[94:95], v[90:91]
	global_load_dwordx4 v[90:93], v[70:71], off offset:1024 nt
	s_waitcnt vmcnt(0)
	v_pk_add_f32 v[92:93], v[96:97], v[92:93]
	v_pk_add_f32 v[90:91], v[94:95], v[90:91]
	v_pk_mul_f32 v[92:93], v[92:93], s[30:31] op_sel_hi:[1,0]
	v_pk_mul_f32 v[90:91], v[90:91], s[30:31] op_sel_hi:[1,0]
	s_nop 0
	v_cvt_pk_bf16_f32 v90, v90, v91
	v_cvt_pk_bf16_f32 v91, v92, v93
.LBB0_1893:
	global_load_dwordx2 v[94:95], v[52:53], off offset:1024 nt
	s_and_b64 vcc, exec, s[34:35]
	s_mov_b64 s[2:3], -1
	s_cbranch_vccnz .LBB0_1897
	global_load_dwordx2 v[92:93], v[50:51], off offset:1024 nt
	s_cbranch_execz .LBB0_1898

.LBB0_1896:
	global_load_dwordx2 v[96:97], v[72:73], off offset:1024 nt
	s_cbranch_execnz .LBB0_1901
	s_branch .LBB0_1900

.LBB0_1898:
	global_load_dwordx4 v[96:99], v[66:67], off offset:2048 nt
	global_load_dwordx4 v[100:103], v[68:69], off offset:2048 nt
	s_waitcnt vmcnt(0)
	v_pk_add_f32 v[92:93], v[98:99], v[102:103]
	v_pk_add_f32 v[100:101], v[96:97], v[100:101]
	global_load_dwordx4 v[96:99], v[64:65], off offset:2048 nt
	s_waitcnt vmcnt(0)
	v_pk_add_f32 v[92:93], v[92:93], v[98:99]
	v_pk_add_f32 v[100:101], v[100:101], v[96:97]
	global_load_dwordx4 v[96:99], v[62:63], off offset:2048 nt
	s_waitcnt vmcnt(0)
	v_pk_add_f32 v[92:93], v[92:93], v[98:99]
	v_pk_add_f32 v[100:101], v[100:101], v[96:97]
	global_load_dwordx4 v[96:99], v[60:61], off offset:2048 nt
	s_waitcnt vmcnt(0)
	v_pk_add_f32 v[92:93], v[92:93], v[98:99]
	v_pk_add_f32 v[100:101], v[100:101], v[96:97]
	global_load_dwordx4 v[96:99], v[58:59], off offset:2048 nt
	s_waitcnt vmcnt(0)
	v_pk_add_f32 v[92:93], v[92:93], v[98:99]
	v_pk_add_f32 v[100:101], v[100:101], v[96:97]
	global_load_dwordx4 v[96:99], v[56:57], off offset:2048 nt
	s_waitcnt vmcnt(0)
	v_pk_add_f32 v[98:99], v[92:93], v[98:99]
	v_pk_add_f32 v[92:93], v[100:101], v[96:97]
	v_pk_mul_f32 v[96:97], v[98:99], s[30:31] op_sel_hi:[1,0]
	v_pk_mul_f32 v[92:93], v[92:93], s[30:31] op_sel_hi:[1,0]
	s_nop 0
	v_cvt_pk_bf16_f32 v92, v92, v93
	v_cvt_pk_bf16_f32 v93, v96, v97
	s_and_b64 vcc, exec, s[36:37]
	s_mov_b64 s[2:3], -1
	s_cbranch_vccz .LBB0_1896

.LBB0_1900:
	global_load_dwordx4 v[96:99], v[84:85], off offset:2048 nt
	global_load_dwordx4 v[100:103], v[86:87], off offset:2048 nt
	s_waitcnt vmcnt(0)
	v_pk_add_f32 v[102:103], v[98:99], v[102:103]
	v_pk_add_f32 v[100:101], v[96:97], v[100:101]
	global_load_dwordx4 v[96:99], v[82:83], off offset:2048 nt
	s_waitcnt vmcnt(0)
	v_pk_add_f32 v[102:103], v[102:103], v[98:99]
	v_pk_add_f32 v[100:101], v[100:101], v[96:97]
	global_load_dwordx4 v[96:99], v[80:81], off offset:2048 nt
	s_waitcnt vmcnt(0)
	v_pk_add_f32 v[102:103], v[102:103], v[98:99]
	v_pk_add_f32 v[100:101], v[100:101], v[96:97]
	global_load_dwordx4 v[96:99], v[76:77], off offset:2048 nt
	s_waitcnt vmcnt(0)
	v_pk_add_f32 v[102:103], v[102:103], v[98:99]
	v_pk_add_f32 v[100:101], v[100:101], v[96:97]
	global_load_dwordx4 v[96:99], v[74:75], off offset:2048 nt
	s_waitcnt vmcnt(0)
	v_pk_add_f32 v[102:103], v[102:103], v[98:99]
	v_pk_add_f32 v[100:101], v[100:101], v[96:97]
	global_load_dwordx4 v[96:99], v[70:71], off offset:2048 nt
	s_waitcnt vmcnt(0)
	v_pk_add_f32 v[98:99], v[102:103], v[98:99]
	v_pk_add_f32 v[96:97], v[100:101], v[96:97]
	v_pk_mul_f32 v[98:99], v[98:99], s[30:31] op_sel_hi:[1,0]
	v_pk_mul_f32 v[96:97], v[96:97], s[30:31] op_sel_hi:[1,0]
	s_nop 0
	v_cvt_pk_bf16_f32 v96, v96, v97
	v_cvt_pk_bf16_f32 v97, v98, v99
.LBB0_1901:
	global_load_dwordx2 v[98:99], v[52:53], off offset:1536 nt
	s_and_b64 vcc, exec, s[34:35]
	s_mov_b64 s[2:3], -1
	s_cbranch_vccnz .LBB0_1905
	global_load_dwordx2 v[52:53], v[50:51], off offset:1536 nt
	s_cbranch_execz .LBB0_1906

.LBB0_1904:
	global_load_dwordx2 v[50:51], v[72:73], off offset:1536 nt
	s_cbranch_execnz .LBB0_1876
	s_branch .LBB0_1908

.LBB0_1906:
	global_load_dwordx4 v[50:53], v[66:67], off offset:3072 nt
	s_nop 0
	global_load_dwordx4 v[66:69], v[68:69], off offset:3072 nt
	s_waitcnt vmcnt(0)
	v_pk_add_f32 v[68:69], v[52:53], v[68:69]
	v_pk_add_f32 v[66:67], v[50:51], v[66:67]
	global_load_dwordx4 v[50:53], v[64:65], off offset:3072 nt
	s_waitcnt vmcnt(0)
	v_pk_add_f32 v[64:65], v[68:69], v[52:53]
	v_pk_add_f32 v[66:67], v[66:67], v[50:51]
	global_load_dwordx4 v[50:53], v[62:63], off offset:3072 nt
	s_waitcnt vmcnt(0)
	v_pk_add_f32 v[62:63], v[64:65], v[52:53]
	v_pk_add_f32 v[64:65], v[66:67], v[50:51]
	global_load_dwordx4 v[50:53], v[60:61], off offset:3072 nt
	s_waitcnt vmcnt(0)
	v_pk_add_f32 v[60:61], v[62:63], v[52:53]
	v_pk_add_f32 v[62:63], v[64:65], v[50:51]
	global_load_dwordx4 v[50:53], v[58:59], off offset:3072 nt
	s_waitcnt vmcnt(0)
	v_pk_add_f32 v[58:59], v[60:61], v[52:53]
	v_pk_add_f32 v[60:61], v[62:63], v[50:51]
	global_load_dwordx4 v[50:53], v[56:57], off offset:3072 nt
	s_waitcnt vmcnt(0)
	v_pk_add_f32 v[50:51], v[60:61], v[50:51]
	v_pk_add_f32 v[56:57], v[58:59], v[52:53]
	v_pk_mul_f32 v[50:51], v[50:51], s[30:31] op_sel_hi:[1,0]
	s_nop 0
	v_cvt_pk_bf16_f32 v52, v50, v51
	v_pk_mul_f32 v[50:51], v[56:57], s[30:31] op_sel_hi:[1,0]
	s_nop 0
	v_cvt_pk_bf16_f32 v53, v50, v51
	s_and_b64 vcc, exec, s[36:37]
	s_mov_b64 s[2:3], -1
	s_cbranch_vccz .LBB0_1904

.LBB0_1908:
	global_load_dwordx4 v[56:59], v[84:85], off offset:3072 nt
	global_load_dwordx4 v[60:63], v[86:87], off offset:3072 nt
	s_waitcnt vmcnt(0)
	v_pk_add_f32 v[50:51], v[58:59], v[62:63]
	v_pk_add_f32 v[60:61], v[56:57], v[60:61]
	global_load_dwordx4 v[56:59], v[82:83], off offset:3072 nt
	s_waitcnt vmcnt(0)
	v_pk_add_f32 v[50:51], v[50:51], v[58:59]
	v_pk_add_f32 v[60:61], v[60:61], v[56:57]
	global_load_dwordx4 v[56:59], v[80:81], off offset:3072 nt
	s_waitcnt vmcnt(0)
	v_pk_add_f32 v[50:51], v[50:51], v[58:59]
	v_pk_add_f32 v[60:61], v[60:61], v[56:57]
	global_load_dwordx4 v[56:59], v[76:77], off offset:3072 nt
	s_waitcnt vmcnt(0)
	v_pk_add_f32 v[50:51], v[50:51], v[58:59]
	v_pk_add_f32 v[60:61], v[60:61], v[56:57]
	global_load_dwordx4 v[56:59], v[74:75], off offset:3072 nt
	s_waitcnt vmcnt(0)
	v_pk_add_f32 v[50:51], v[50:51], v[58:59]
	v_pk_add_f32 v[60:61], v[60:61], v[56:57]
	global_load_dwordx4 v[56:59], v[70:71], off offset:3072 nt
	s_waitcnt vmcnt(0)
	v_pk_add_f32 v[58:59], v[50:51], v[58:59]
	v_pk_add_f32 v[50:51], v[60:61], v[56:57]
	v_pk_mul_f32 v[56:57], v[58:59], s[30:31] op_sel_hi:[1,0]
	v_pk_mul_f32 v[50:51], v[50:51], s[30:31] op_sel_hi:[1,0]
	s_nop 0
	v_cvt_pk_bf16_f32 v50, v50, v51
	v_cvt_pk_bf16_f32 v51, v56, v57
	s_branch .LBB0_1876
